# gemm8 rotary block rewritten by hand (scalar f32 ops in place, no packed-op shuffles), on top of the de-branched pack phase
# speedup vs baseline: 1.0147x; 1.0039x over previous
.LBB15_13:
	v_lshl_or_b32 v139, v135, 2, v146
	s_and_b32 s2, s6, 0x700
	v_or3_b32 v156, v134, s2, v144
	v_or_b32_e32 v130, 16, v156
	v_or_b32_e32 v131, 0x80, v156
	v_or_b32_e32 v132, 0x90, v156
	v_cvt_f32_u32_e32 v160, v156
	v_cvt_f32_u32_e32 v161, v130
	v_cvt_f32_u32_e32 v162, v131
	v_cvt_f32_u32_e32 v163, v132
	v_cvt_f32_ubyte0_e32 v130, v139
	v_or_b32_e32 v131, 1, v139
	v_cvt_f32_ubyte0_e32 v131, v131
	v_or_b32_e32 v132, 2, v139
	v_cvt_f32_ubyte0_e32 v132, v132
	v_or_b32_e32 v133, 3, v139
	v_cvt_f32_ubyte0_e32 v133, v133
	v_mul_f32_e32 v130, 0xbdd49a78, v130
	v_mul_f32_e32 v131, 0xbdd49a78, v131
	v_mul_f32_e32 v132, 0xbdd49a78, v132
	v_mul_f32_e32 v133, 0xbdd49a78, v133
	v_exp_f32_e32 v164, v130
	v_exp_f32_e32 v165, v131
	v_exp_f32_e32 v166, v132
	v_exp_f32_e32 v167, v133
	v_mul_f32_e32 v164, 0.15915494, v164
	v_mul_f32_e32 v165, 0.15915494, v165
	v_mul_f32_e32 v166, 0.15915494, v166
	v_mul_f32_e32 v167, 0.15915494, v167
	v_mul_f32_e32 v130, v160, v164
	v_mul_f32_e32 v131, v160, v165
	v_mul_f32_e32 v132, v160, v166
	v_mul_f32_e32 v133, v160, v167
	v_fract_f32_e32 v130, v130
	v_fract_f32_e32 v131, v131
	v_fract_f32_e32 v132, v132
	v_fract_f32_e32 v133, v133
	v_cos_f32_e32 v137, v130
	v_cos_f32_e32 v138, v131
	v_cos_f32_e32 v140, v132
	v_cos_f32_e32 v141, v133
	v_sin_f32_e32 v142, v130
	v_sin_f32_e32 v143, v131
	v_sin_f32_e32 v146, v132
	v_sin_f32_e32 v147, v133
	v_mul_f32_e32 v148, v62, v142
	v_mul_f32_e32 v149, v63, v143
	v_mul_f32_e32 v150, v64, v146
	v_mul_f32_e32 v151, v65, v147
	v_mul_f32_e32 v152, v126, v142
	v_mul_f32_e32 v153, v127, v143
	v_mul_f32_e32 v154, v128, v146
	v_mul_f32_e32 v155, v129, v147
	v_fma_f32 v126, v126, v137, -v148
	v_fma_f32 v127, v127, v138, -v149
	v_fma_f32 v128, v128, v140, -v150
	v_fma_f32 v129, v129, v141, -v151
	v_fma_f32 v62, v62, v137, v152
	v_fma_f32 v63, v63, v138, v153
	v_fma_f32 v64, v64, v140, v154
	v_fma_f32 v65, v65, v141, v155
	v_mul_f32_e32 v130, v161, v164
	v_mul_f32_e32 v131, v161, v165
	v_mul_f32_e32 v132, v161, v166
	v_mul_f32_e32 v133, v161, v167
	v_fract_f32_e32 v130, v130
	v_fract_f32_e32 v131, v131
	v_fract_f32_e32 v132, v132
	v_fract_f32_e32 v133, v133
	v_cos_f32_e32 v137, v130
	v_cos_f32_e32 v138, v131
	v_cos_f32_e32 v140, v132
	v_cos_f32_e32 v141, v133
	v_sin_f32_e32 v142, v130
	v_sin_f32_e32 v143, v131
	v_sin_f32_e32 v146, v132
	v_sin_f32_e32 v147, v133
	v_mul_f32_e32 v148, v58, v142
	v_mul_f32_e32 v149, v59, v143
	v_mul_f32_e32 v150, v60, v146
	v_mul_f32_e32 v151, v61, v147
	v_mul_f32_e32 v152, v122, v142
	v_mul_f32_e32 v153, v123, v143
	v_mul_f32_e32 v154, v124, v146
	v_mul_f32_e32 v155, v125, v147
	v_fma_f32 v122, v122, v137, -v148
	v_fma_f32 v123, v123, v138, -v149
	v_fma_f32 v124, v124, v140, -v150
	v_fma_f32 v125, v125, v141, -v151
	v_fma_f32 v58, v58, v137, v152
	v_fma_f32 v59, v59, v138, v153
	v_fma_f32 v60, v60, v140, v154
	v_fma_f32 v61, v61, v141, v155
	v_mul_f32_e32 v130, v162, v164
	v_mul_f32_e32 v131, v162, v165
	v_mul_f32_e32 v132, v162, v166
	v_mul_f32_e32 v133, v162, v167
	v_fract_f32_e32 v130, v130
	v_fract_f32_e32 v131, v131
	v_fract_f32_e32 v132, v132
	v_fract_f32_e32 v133, v133
	v_cos_f32_e32 v137, v130
	v_cos_f32_e32 v138, v131
	v_cos_f32_e32 v140, v132
	v_cos_f32_e32 v141, v133
	v_sin_f32_e32 v142, v130
	v_sin_f32_e32 v143, v131
	v_sin_f32_e32 v146, v132
	v_sin_f32_e32 v147, v133
	v_mul_f32_e32 v148, v30, v142
	v_mul_f32_e32 v149, v31, v143
	v_mul_f32_e32 v150, v32, v146
	v_mul_f32_e32 v151, v33, v147
	v_mul_f32_e32 v152, v94, v142
	v_mul_f32_e32 v153, v95, v143
	v_mul_f32_e32 v154, v96, v146
	v_mul_f32_e32 v155, v97, v147
	v_fma_f32 v94, v94, v137, -v148
	v_fma_f32 v95, v95, v138, -v149
	v_fma_f32 v96, v96, v140, -v150
	v_fma_f32 v97, v97, v141, -v151
	v_fma_f32 v30, v30, v137, v152
	v_fma_f32 v31, v31, v138, v153
	v_fma_f32 v32, v32, v140, v154
	v_fma_f32 v33, v33, v141, v155
	v_mul_f32_e32 v130, v163, v164
	v_mul_f32_e32 v131, v163, v165
	v_mul_f32_e32 v132, v163, v166
	v_mul_f32_e32 v133, v163, v167
	v_fract_f32_e32 v130, v130
	v_fract_f32_e32 v131, v131
	v_fract_f32_e32 v132, v132
	v_fract_f32_e32 v133, v133
	v_cos_f32_e32 v137, v130
	v_cos_f32_e32 v138, v131
	v_cos_f32_e32 v140, v132
	v_cos_f32_e32 v141, v133
	v_sin_f32_e32 v142, v130
	v_sin_f32_e32 v143, v131
	v_sin_f32_e32 v146, v132
	v_sin_f32_e32 v147, v133
	v_mul_f32_e32 v148, v26, v142
	v_mul_f32_e32 v149, v27, v143
	v_mul_f32_e32 v150, v28, v146
	v_mul_f32_e32 v151, v29, v147
	v_mul_f32_e32 v152, v90, v142
	v_mul_f32_e32 v153, v91, v143
	v_mul_f32_e32 v154, v92, v146
	v_mul_f32_e32 v155, v93, v147
	v_fma_f32 v90, v90, v137, -v148
	v_fma_f32 v91, v91, v138, -v149
	v_fma_f32 v92, v92, v140, -v150
	v_fma_f32 v93, v93, v141, -v151
	v_fma_f32 v26, v26, v137, v152
	v_fma_f32 v27, v27, v138, v153
	v_fma_f32 v28, v28, v140, v154
	v_fma_f32 v29, v29, v141, v155
	v_or_b32_e32 v130, 16, v139
	v_cvt_f32_ubyte0_e32 v130, v130
	v_or_b32_e32 v131, 17, v139
	v_cvt_f32_ubyte0_e32 v131, v131
	v_or_b32_e32 v132, 18, v139
	v_cvt_f32_ubyte0_e32 v132, v132
	v_or_b32_e32 v133, 19, v139
	v_cvt_f32_ubyte0_e32 v133, v133
	v_mul_f32_e32 v130, 0xbdd49a78, v130
	v_mul_f32_e32 v131, 0xbdd49a78, v131
	v_mul_f32_e32 v132, 0xbdd49a78, v132
	v_mul_f32_e32 v133, 0xbdd49a78, v133
	v_exp_f32_e32 v164, v130
	v_exp_f32_e32 v165, v131
	v_exp_f32_e32 v166, v132
	v_exp_f32_e32 v167, v133
	v_mul_f32_e32 v164, 0.15915494, v164
	v_mul_f32_e32 v165, 0.15915494, v165
	v_mul_f32_e32 v166, 0.15915494, v166
	v_mul_f32_e32 v167, 0.15915494, v167
	v_mul_f32_e32 v130, v160, v164
	v_mul_f32_e32 v131, v160, v165
	v_mul_f32_e32 v132, v160, v166
	v_mul_f32_e32 v133, v160, v167
	v_fract_f32_e32 v130, v130
	v_fract_f32_e32 v131, v131
	v_fract_f32_e32 v132, v132
	v_fract_f32_e32 v133, v133
	v_cos_f32_e32 v137, v130
	v_cos_f32_e32 v138, v131
	v_cos_f32_e32 v140, v132
	v_cos_f32_e32 v141, v133
	v_sin_f32_e32 v142, v130
	v_sin_f32_e32 v143, v131
	v_sin_f32_e32 v146, v132
	v_sin_f32_e32 v147, v133
	v_mul_f32_e32 v148, v54, v142
	v_mul_f32_e32 v149, v55, v143
	v_mul_f32_e32 v150, v56, v146
	v_mul_f32_e32 v151, v57, v147
	v_mul_f32_e32 v152, v118, v142
	v_mul_f32_e32 v153, v119, v143
	v_mul_f32_e32 v154, v120, v146
	v_mul_f32_e32 v155, v121, v147
	v_fma_f32 v118, v118, v137, -v148
	v_fma_f32 v119, v119, v138, -v149
	v_fma_f32 v120, v120, v140, -v150
	v_fma_f32 v121, v121, v141, -v151
	v_fma_f32 v54, v54, v137, v152
	v_fma_f32 v55, v55, v138, v153
	v_fma_f32 v56, v56, v140, v154
	v_fma_f32 v57, v57, v141, v155
	v_mul_f32_e32 v130, v161, v164
	v_mul_f32_e32 v131, v161, v165
	v_mul_f32_e32 v132, v161, v166
	v_mul_f32_e32 v133, v161, v167
	v_fract_f32_e32 v130, v130
	v_fract_f32_e32 v131, v131
	v_fract_f32_e32 v132, v132
	v_fract_f32_e32 v133, v133
	v_cos_f32_e32 v137, v130
	v_cos_f32_e32 v138, v131
	v_cos_f32_e32 v140, v132
	v_cos_f32_e32 v141, v133
	v_sin_f32_e32 v142, v130
	v_sin_f32_e32 v143, v131
	v_sin_f32_e32 v146, v132
	v_sin_f32_e32 v147, v133
	v_mul_f32_e32 v148, v50, v142
	v_mul_f32_e32 v149, v51, v143
	v_mul_f32_e32 v150, v52, v146
	v_mul_f32_e32 v151, v53, v147
	v_mul_f32_e32 v152, v114, v142
	v_mul_f32_e32 v153, v115, v143
	v_mul_f32_e32 v154, v116, v146
	v_mul_f32_e32 v155, v117, v147
	v_fma_f32 v114, v114, v137, -v148
	v_fma_f32 v115, v115, v138, -v149
	v_fma_f32 v116, v116, v140, -v150
	v_fma_f32 v117, v117, v141, -v151
	v_fma_f32 v50, v50, v137, v152
	v_fma_f32 v51, v51, v138, v153
	v_fma_f32 v52, v52, v140, v154
	v_fma_f32 v53, v53, v141, v155
	v_mul_f32_e32 v130, v162, v164
	v_mul_f32_e32 v131, v162, v165
	v_mul_f32_e32 v132, v162, v166
	v_mul_f32_e32 v133, v162, v167
	v_fract_f32_e32 v130, v130
	v_fract_f32_e32 v131, v131
	v_fract_f32_e32 v132, v132
	v_fract_f32_e32 v133, v133
	v_cos_f32_e32 v137, v130
	v_cos_f32_e32 v138, v131
	v_cos_f32_e32 v140, v132
	v_cos_f32_e32 v141, v133
	v_sin_f32_e32 v142, v130
	v_sin_f32_e32 v143, v131
	v_sin_f32_e32 v146, v132
	v_sin_f32_e32 v147, v133
	v_mul_f32_e32 v148, v22, v142
	v_mul_f32_e32 v149, v23, v143
	v_mul_f32_e32 v150, v24, v146
	v_mul_f32_e32 v151, v25, v147
	v_mul_f32_e32 v152, v86, v142
	v_mul_f32_e32 v153, v87, v143
	v_mul_f32_e32 v154, v88, v146
	v_mul_f32_e32 v155, v89, v147
	v_fma_f32 v86, v86, v137, -v148
	v_fma_f32 v87, v87, v138, -v149
	v_fma_f32 v88, v88, v140, -v150
	v_fma_f32 v89, v89, v141, -v151
	v_fma_f32 v22, v22, v137, v152
	v_fma_f32 v23, v23, v138, v153
	v_fma_f32 v24, v24, v140, v154
	v_fma_f32 v25, v25, v141, v155
	v_mul_f32_e32 v130, v163, v164
	v_mul_f32_e32 v131, v163, v165
	v_mul_f32_e32 v132, v163, v166
	v_mul_f32_e32 v133, v163, v167
	v_fract_f32_e32 v130, v130
	v_fract_f32_e32 v131, v131
	v_fract_f32_e32 v132, v132
	v_fract_f32_e32 v133, v133
	v_cos_f32_e32 v137, v130
	v_cos_f32_e32 v138, v131
	v_cos_f32_e32 v140, v132
	v_cos_f32_e32 v141, v133
	v_sin_f32_e32 v142, v130
	v_sin_f32_e32 v143, v131
	v_sin_f32_e32 v146, v132
	v_sin_f32_e32 v147, v133
	v_mul_f32_e32 v148, v18, v142
	v_mul_f32_e32 v149, v19, v143
	v_mul_f32_e32 v150, v20, v146
	v_mul_f32_e32 v151, v21, v147
	v_mul_f32_e32 v152, v82, v142
	v_mul_f32_e32 v153, v83, v143
	v_mul_f32_e32 v154, v84, v146
	v_mul_f32_e32 v155, v85, v147
	v_fma_f32 v82, v82, v137, -v148
	v_fma_f32 v83, v83, v138, -v149
	v_fma_f32 v84, v84, v140, -v150
	v_fma_f32 v85, v85, v141, -v151
	v_fma_f32 v18, v18, v137, v152
	v_fma_f32 v19, v19, v138, v153
	v_fma_f32 v20, v20, v140, v154
	v_fma_f32 v21, v21, v141, v155
	v_or_b32_e32 v130, 32, v139
	v_cvt_f32_ubyte0_e32 v130, v130
	v_or_b32_e32 v131, 33, v139
	v_cvt_f32_ubyte0_e32 v131, v131
	v_or_b32_e32 v132, 34, v139
	v_cvt_f32_ubyte0_e32 v132, v132
	v_or_b32_e32 v133, 35, v139
	v_cvt_f32_ubyte0_e32 v133, v133
	v_mul_f32_e32 v130, 0xbdd49a78, v130
	v_mul_f32_e32 v131, 0xbdd49a78, v131
	v_mul_f32_e32 v132, 0xbdd49a78, v132
	v_mul_f32_e32 v133, 0xbdd49a78, v133
	v_exp_f32_e32 v164, v130
	v_exp_f32_e32 v165, v131
	v_exp_f32_e32 v166, v132
	v_exp_f32_e32 v167, v133
	v_mul_f32_e32 v164, 0.15915494, v164
	v_mul_f32_e32 v165, 0.15915494, v165
	v_mul_f32_e32 v166, 0.15915494, v166
	v_mul_f32_e32 v167, 0.15915494, v167
	v_mul_f32_e32 v130, v160, v164
	v_mul_f32_e32 v131, v160, v165
	v_mul_f32_e32 v132, v160, v166
	v_mul_f32_e32 v133, v160, v167
	v_fract_f32_e32 v130, v130
	v_fract_f32_e32 v131, v131
	v_fract_f32_e32 v132, v132
	v_fract_f32_e32 v133, v133
	v_cos_f32_e32 v137, v130
	v_cos_f32_e32 v138, v131
	v_cos_f32_e32 v140, v132
	v_cos_f32_e32 v141, v133
	v_sin_f32_e32 v142, v130
	v_sin_f32_e32 v143, v131
	v_sin_f32_e32 v146, v132
	v_sin_f32_e32 v147, v133
	v_mul_f32_e32 v148, v46, v142
	v_mul_f32_e32 v149, v47, v143
	v_mul_f32_e32 v150, v48, v146
	v_mul_f32_e32 v151, v49, v147
	v_mul_f32_e32 v152, v110, v142
	v_mul_f32_e32 v153, v111, v143
	v_mul_f32_e32 v154, v112, v146
	v_mul_f32_e32 v155, v113, v147
	v_fma_f32 v110, v110, v137, -v148
	v_fma_f32 v111, v111, v138, -v149
	v_fma_f32 v112, v112, v140, -v150
	v_fma_f32 v113, v113, v141, -v151
	v_fma_f32 v46, v46, v137, v152
	v_fma_f32 v47, v47, v138, v153
	v_fma_f32 v48, v48, v140, v154
	v_fma_f32 v49, v49, v141, v155
	v_mul_f32_e32 v130, v161, v164
	v_mul_f32_e32 v131, v161, v165
	v_mul_f32_e32 v132, v161, v166
	v_mul_f32_e32 v133, v161, v167
	v_fract_f32_e32 v130, v130
	v_fract_f32_e32 v131, v131
	v_fract_f32_e32 v132, v132
	v_fract_f32_e32 v133, v133
	v_cos_f32_e32 v137, v130
	v_cos_f32_e32 v138, v131
	v_cos_f32_e32 v140, v132
	v_cos_f32_e32 v141, v133
	v_sin_f32_e32 v142, v130
	v_sin_f32_e32 v143, v131
	v_sin_f32_e32 v146, v132
	v_sin_f32_e32 v147, v133
	v_mul_f32_e32 v148, v42, v142
	v_mul_f32_e32 v149, v43, v143
	v_mul_f32_e32 v150, v44, v146
	v_mul_f32_e32 v151, v45, v147
	v_mul_f32_e32 v152, v106, v142
	v_mul_f32_e32 v153, v107, v143
	v_mul_f32_e32 v154, v108, v146
	v_mul_f32_e32 v155, v109, v147
	v_fma_f32 v106, v106, v137, -v148
	v_fma_f32 v107, v107, v138, -v149
	v_fma_f32 v108, v108, v140, -v150
	v_fma_f32 v109, v109, v141, -v151
	v_fma_f32 v42, v42, v137, v152
	v_fma_f32 v43, v43, v138, v153
	v_fma_f32 v44, v44, v140, v154
	v_fma_f32 v45, v45, v141, v155
	v_mul_f32_e32 v130, v162, v164
	v_mul_f32_e32 v131, v162, v165
	v_mul_f32_e32 v132, v162, v166
	v_mul_f32_e32 v133, v162, v167
	v_fract_f32_e32 v130, v130
	v_fract_f32_e32 v131, v131
	v_fract_f32_e32 v132, v132
	v_fract_f32_e32 v133, v133
	v_cos_f32_e32 v137, v130
	v_cos_f32_e32 v138, v131
	v_cos_f32_e32 v140, v132
	v_cos_f32_e32 v141, v133
	v_sin_f32_e32 v142, v130
	v_sin_f32_e32 v143, v131
	v_sin_f32_e32 v146, v132
	v_sin_f32_e32 v147, v133
	v_mul_f32_e32 v148, v14, v142
	v_mul_f32_e32 v149, v15, v143
	v_mul_f32_e32 v150, v16, v146
	v_mul_f32_e32 v151, v17, v147
	v_mul_f32_e32 v152, v78, v142
	v_mul_f32_e32 v153, v79, v143
	v_mul_f32_e32 v154, v80, v146
	v_mul_f32_e32 v155, v81, v147
	v_fma_f32 v78, v78, v137, -v148
	v_fma_f32 v79, v79, v138, -v149
	v_fma_f32 v80, v80, v140, -v150
	v_fma_f32 v81, v81, v141, -v151
	v_fma_f32 v14, v14, v137, v152
	v_fma_f32 v15, v15, v138, v153
	v_fma_f32 v16, v16, v140, v154
	v_fma_f32 v17, v17, v141, v155
	v_mul_f32_e32 v130, v163, v164
	v_mul_f32_e32 v131, v163, v165
	v_mul_f32_e32 v132, v163, v166
	v_mul_f32_e32 v133, v163, v167
	v_fract_f32_e32 v130, v130
	v_fract_f32_e32 v131, v131
	v_fract_f32_e32 v132, v132
	v_fract_f32_e32 v133, v133
	v_cos_f32_e32 v137, v130
	v_cos_f32_e32 v138, v131
	v_cos_f32_e32 v140, v132
	v_cos_f32_e32 v141, v133
	v_sin_f32_e32 v142, v130
	v_sin_f32_e32 v143, v131
	v_sin_f32_e32 v146, v132
	v_sin_f32_e32 v147, v133
	v_mul_f32_e32 v148, v10, v142
	v_mul_f32_e32 v149, v11, v143
	v_mul_f32_e32 v150, v12, v146
	v_mul_f32_e32 v151, v13, v147
	v_mul_f32_e32 v152, v74, v142
	v_mul_f32_e32 v153, v75, v143
	v_mul_f32_e32 v154, v76, v146
	v_mul_f32_e32 v155, v77, v147
	v_fma_f32 v74, v74, v137, -v148
	v_fma_f32 v75, v75, v138, -v149
	v_fma_f32 v76, v76, v140, -v150
	v_fma_f32 v77, v77, v141, -v151
	v_fma_f32 v10, v10, v137, v152
	v_fma_f32 v11, v11, v138, v153
	v_fma_f32 v12, v12, v140, v154
	v_fma_f32 v13, v13, v141, v155
	v_or_b32_e32 v130, 48, v139
	v_cvt_f32_ubyte0_e32 v130, v130
	v_or_b32_e32 v131, 49, v139
	v_cvt_f32_ubyte0_e32 v131, v131
	v_or_b32_e32 v132, 50, v139
	v_cvt_f32_ubyte0_e32 v132, v132
	v_or_b32_e32 v133, 51, v139
	v_cvt_f32_ubyte0_e32 v133, v133
	v_mul_f32_e32 v130, 0xbdd49a78, v130
	v_mul_f32_e32 v131, 0xbdd49a78, v131
	v_mul_f32_e32 v132, 0xbdd49a78, v132
	v_mul_f32_e32 v133, 0xbdd49a78, v133
	v_exp_f32_e32 v164, v130
	v_exp_f32_e32 v165, v131
	v_exp_f32_e32 v166, v132
	v_exp_f32_e32 v167, v133
	v_mul_f32_e32 v164, 0.15915494, v164
	v_mul_f32_e32 v165, 0.15915494, v165
	v_mul_f32_e32 v166, 0.15915494, v166
	v_mul_f32_e32 v167, 0.15915494, v167
	v_mul_f32_e32 v130, v160, v164
	v_mul_f32_e32 v131, v160, v165
	v_mul_f32_e32 v132, v160, v166
	v_mul_f32_e32 v133, v160, v167
	v_fract_f32_e32 v130, v130
	v_fract_f32_e32 v131, v131
	v_fract_f32_e32 v132, v132
	v_fract_f32_e32 v133, v133
	v_cos_f32_e32 v137, v130
	v_cos_f32_e32 v138, v131
	v_cos_f32_e32 v140, v132
	v_cos_f32_e32 v141, v133
	v_sin_f32_e32 v142, v130
	v_sin_f32_e32 v143, v131
	v_sin_f32_e32 v146, v132
	v_sin_f32_e32 v147, v133
	v_mul_f32_e32 v148, v38, v142
	v_mul_f32_e32 v149, v39, v143
	v_mul_f32_e32 v150, v40, v146
	v_mul_f32_e32 v151, v41, v147
	v_mul_f32_e32 v152, v102, v142
	v_mul_f32_e32 v153, v103, v143
	v_mul_f32_e32 v154, v104, v146
	v_mul_f32_e32 v155, v105, v147
	v_fma_f32 v102, v102, v137, -v148
	v_fma_f32 v103, v103, v138, -v149
	v_fma_f32 v104, v104, v140, -v150
	v_fma_f32 v105, v105, v141, -v151
	v_fma_f32 v38, v38, v137, v152
	v_fma_f32 v39, v39, v138, v153
	v_fma_f32 v40, v40, v140, v154
	v_fma_f32 v41, v41, v141, v155
	v_mul_f32_e32 v130, v161, v164
	v_mul_f32_e32 v131, v161, v165
	v_mul_f32_e32 v132, v161, v166
	v_mul_f32_e32 v133, v161, v167
	v_fract_f32_e32 v130, v130
	v_fract_f32_e32 v131, v131
	v_fract_f32_e32 v132, v132
	v_fract_f32_e32 v133, v133
	v_cos_f32_e32 v137, v130
	v_cos_f32_e32 v138, v131
	v_cos_f32_e32 v140, v132
	v_cos_f32_e32 v141, v133
	v_sin_f32_e32 v142, v130
	v_sin_f32_e32 v143, v131
	v_sin_f32_e32 v146, v132
	v_sin_f32_e32 v147, v133
	v_mul_f32_e32 v148, v34, v142
	v_mul_f32_e32 v149, v35, v143
	v_mul_f32_e32 v150, v36, v146
	v_mul_f32_e32 v151, v37, v147
	v_mul_f32_e32 v152, v98, v142
	v_mul_f32_e32 v153, v99, v143
	v_mul_f32_e32 v154, v100, v146
	v_mul_f32_e32 v155, v101, v147
	v_fma_f32 v98, v98, v137, -v148
	v_fma_f32 v99, v99, v138, -v149
	v_fma_f32 v100, v100, v140, -v150
	v_fma_f32 v101, v101, v141, -v151
	v_fma_f32 v34, v34, v137, v152
	v_fma_f32 v35, v35, v138, v153
	v_fma_f32 v36, v36, v140, v154
	v_fma_f32 v37, v37, v141, v155
	v_mul_f32_e32 v130, v162, v164
	v_mul_f32_e32 v131, v162, v165
	v_mul_f32_e32 v132, v162, v166
	v_mul_f32_e32 v133, v162, v167
	v_fract_f32_e32 v130, v130
	v_fract_f32_e32 v131, v131
	v_fract_f32_e32 v132, v132
	v_fract_f32_e32 v133, v133
	v_cos_f32_e32 v137, v130
	v_cos_f32_e32 v138, v131
	v_cos_f32_e32 v140, v132
	v_cos_f32_e32 v141, v133
	v_sin_f32_e32 v142, v130
	v_sin_f32_e32 v143, v131
	v_sin_f32_e32 v146, v132
	v_sin_f32_e32 v147, v133
	v_mul_f32_e32 v148, v6, v142
	v_mul_f32_e32 v149, v7, v143
	v_mul_f32_e32 v150, v8, v146
	v_mul_f32_e32 v151, v9, v147
	v_mul_f32_e32 v152, v70, v142
	v_mul_f32_e32 v153, v71, v143
	v_mul_f32_e32 v154, v72, v146
	v_mul_f32_e32 v155, v73, v147
	v_fma_f32 v70, v70, v137, -v148
	v_fma_f32 v71, v71, v138, -v149
	v_fma_f32 v72, v72, v140, -v150
	v_fma_f32 v73, v73, v141, -v151
	v_fma_f32 v6, v6, v137, v152
	v_fma_f32 v7, v7, v138, v153
	v_fma_f32 v8, v8, v140, v154
	v_fma_f32 v9, v9, v141, v155
	v_mul_f32_e32 v130, v163, v164
	v_mul_f32_e32 v131, v163, v165
	v_mul_f32_e32 v132, v163, v166
	v_mul_f32_e32 v133, v163, v167
	v_fract_f32_e32 v130, v130
	v_fract_f32_e32 v131, v131
	v_fract_f32_e32 v132, v132
	v_fract_f32_e32 v133, v133
	v_cos_f32_e32 v137, v130
	v_cos_f32_e32 v138, v131
	v_cos_f32_e32 v140, v132
	v_cos_f32_e32 v141, v133
	v_sin_f32_e32 v142, v130
	v_sin_f32_e32 v143, v131
	v_sin_f32_e32 v146, v132
	v_sin_f32_e32 v147, v133
	v_mul_f32_e32 v148, v2, v142
	v_mul_f32_e32 v149, v3, v143
	v_mul_f32_e32 v150, v4, v146
	v_mul_f32_e32 v151, v5, v147
	v_mul_f32_e32 v152, v66, v142
	v_mul_f32_e32 v153, v67, v143
	v_mul_f32_e32 v154, v68, v146
	v_mul_f32_e32 v155, v69, v147
	v_fma_f32 v66, v66, v137, -v148
	v_fma_f32 v67, v67, v138, -v149
	v_fma_f32 v68, v68, v140, -v150
	v_fma_f32 v69, v69, v141, -v151
	v_fma_f32 v2, v2, v137, v152
	v_fma_f32 v3, v3, v138, v153
	v_fma_f32 v4, v4, v140, v154
	v_fma_f32 v5, v5, v141, v155
	v_mov_b32_e32 v136, v134
